# v21 plus early L2 write-back issued by every workgroup at grid-barrier arrival
# baseline (speedup 1.0000x reference)
; __device__ __forceinline__ unsigned xb_ld(unsigned* p)              { return __hip_atomic_load(p, __ATOMIC_RELAXED, __HIP_MEMORY_SCOPE_AGENT); }
; __device__ __forceinline__ void xcd_barrier_complete(unsigned* bar, unsigned x, unsigned& nloc, unsigned& nx) {
;     const unsigned G = gridDim.x * gridDim.y * gridDim.z;
;     unsigned sum, cnt, mine, sp = 0u;
;     for (;;) {
;         sum = 0u; cnt = 0u; mine = 0u;
; #pragma unroll
;         for (unsigned j = 0; j < 16; ++j) { const unsigned c = xb_ld(&bar[XB_XCNT(j)]); sum += c; cnt += (c > 0u) ? 1u : 0u; mine = (j == x) ? c : mine; }
; __device__ __forceinline__ void xcd_barrier(const XcdBarrier& b) {
;     asm volatile("s_waitcnt vmcnt(0)" ::: "memory");
;     __syncthreads();
;     if (threadIdx.x == 0) {
;         unsigned* bar = b.bar;
;         __builtin_amdgcn_s_waitcnt(0);
;         unsigned nloc = b.st[0], nx = b.st[1];
;         if (nloc == 0u) { xcd_barrier_complete(bar, b.x, nloc, nx); b.st[0] = nloc; b.st[1] = nx; }
.LBB0_212:
	s_or_b64 exec, exec, s[6:7]
	s_waitcnt vmcnt(0)
	s_barrier
	s_mov_b64 s[4:5], exec
	v_readlane_b32 s0, v252, 5
	v_readlane_b32 s1, v252, 6
	s_and_b64 s[0:1], s[4:5], s[0:1]
	s_mov_b64 exec, s[0:1]
	s_cbranch_execz .LBB0_264
	s_add_i32 s0, 0, 0x26c00
	v_mov_b32_e32 v1, s0
	s_waitcnt vmcnt(0) expcnt(0) lgkmcnt(0)
	buffer_wbl2 sc1
	ds_read_b32 v3, v1
	s_add_i32 s0, 0, 0x26c04
	v_mov_b32_e32 v1, s0
	ds_read_b32 v1, v1
	s_waitcnt lgkmcnt(1)
	v_cmp_ne_u32_e32 vcc, 0, v3
	s_cbranch_vccnz .LBB0_228
	v_readlane_b32 s2, v252, 7
	v_readlane_b32 s3, v252, 8
	s_load_dwordx2 s[0:1], s[2:3], 0x4
	v_readlane_b32 s2, v252, 0
	v_readlane_b32 s3, v252, 1
	s_add_u32 s6, s2, 0x4200
	s_addc_u32 s7, s3, 0
	s_add_u32 s8, s2, 0x4400
	s_addc_u32 s9, s3, 0
	s_add_u32 s10, s2, 0x4500
	s_addc_u32 s11, s3, 0
	s_add_u32 s12, s2, 0x4600
	s_addc_u32 s13, s3, 0
	s_add_u32 s14, s2, 0x4700
	s_addc_u32 s15, s3, 0
	s_add_u32 s16, s2, 0x4800
	s_addc_u32 s17, s3, 0
	s_add_u32 s18, s2, 0x4900
	s_addc_u32 s19, s3, 0
	s_add_u32 s20, s2, 0x4a00
	s_addc_u32 s21, s3, 0
	s_add_u32 s24, s2, 0x4b00
	s_addc_u32 s25, s3, 0
	s_add_u32 s34, s2, 0x4c00
	s_addc_u32 s35, s3, 0
	s_add_u32 s36, s2, 0x4d00
	s_addc_u32 s37, s3, 0
	s_add_u32 s38, s2, 0x4e00
	s_addc_u32 s39, s3, 0
	s_add_u32 s40, s2, 0x4f00
	s_addc_u32 s41, s3, 0
	s_add_u32 s42, s2, 0x5000
	s_addc_u32 s43, s3, 0
	s_add_u32 s44, s2, 0x5100
	s_addc_u32 s45, s3, 0
	s_add_u32 s46, s2, 0x5200
	s_addc_u32 s47, s3, 0
	s_waitcnt lgkmcnt(0)
	s_mul_i32 s0, s0, s78
	s_add_u32 s48, s2, 0x5300
	s_mul_i32 s0, s0, s1
	s_addc_u32 s49, s3, 0
	s_mov_b32 s1, 1
	v_mov_b32_e32 v17, 0
	s_branch .LBB0_216

; __device__ __forceinline__ void xcd_barrier(const XcdBarrier& b) {
;     asm volatile("s_waitcnt vmcnt(0)" ::: "memory");
;     __syncthreads();
;     if (threadIdx.x == 0) {
;         unsigned* bar = b.bar;
;         __builtin_amdgcn_s_waitcnt(0);
;         unsigned nloc = b.st[0], nx = b.st[1];
;         if (nloc == 0u) { xcd_barrier_complete(bar, b.x, nloc, nx); b.st[0] = nloc; b.st[1] = nx; }
.LBB0_296:
	s_waitcnt vmcnt(0)
	s_waitcnt vmcnt(0)
	s_barrier
	s_mov_b64 s[4:5], exec
	v_readlane_b32 s0, v252, 5
	v_readlane_b32 s1, v252, 6
	s_and_b64 s[0:1], s[4:5], s[0:1]
	s_mov_b64 exec, s[0:1]
	s_cbranch_execz .LBB0_348
	s_add_i32 s0, 0, 0x26c00
	v_mov_b32_e32 v1, s0
	s_waitcnt vmcnt(0) expcnt(0) lgkmcnt(0)
	buffer_wbl2 sc1
	ds_read_b32 v3, v1
	s_add_i32 s0, 0, 0x26c04
	v_mov_b32_e32 v1, s0
	ds_read_b32 v1, v1
	s_waitcnt lgkmcnt(1)
	v_cmp_ne_u32_e32 vcc, 0, v3
	s_cbranch_vccnz .LBB0_312
	v_readlane_b32 s2, v252, 7
	v_readlane_b32 s3, v252, 8
	s_load_dwordx2 s[0:1], s[2:3], 0x4
	v_readlane_b32 s2, v252, 0
	v_readlane_b32 s3, v252, 1
	s_add_u32 s6, s2, 0x4200
	s_addc_u32 s7, s3, 0
	s_add_u32 s8, s2, 0x4400
	s_addc_u32 s9, s3, 0
	s_add_u32 s10, s2, 0x4500
	s_addc_u32 s11, s3, 0
	s_add_u32 s12, s2, 0x4600
	s_addc_u32 s13, s3, 0
	s_add_u32 s14, s2, 0x4700
	s_addc_u32 s15, s3, 0
	s_add_u32 s16, s2, 0x4800
	s_addc_u32 s17, s3, 0
	s_add_u32 s18, s2, 0x4900
	s_addc_u32 s19, s3, 0
	s_add_u32 s20, s2, 0x4a00
	s_addc_u32 s21, s3, 0
	s_add_u32 s24, s2, 0x4b00
	s_addc_u32 s25, s3, 0
	s_add_u32 s34, s2, 0x4c00
	s_addc_u32 s35, s3, 0
	s_add_u32 s36, s2, 0x4d00
	s_addc_u32 s37, s3, 0
	s_add_u32 s38, s2, 0x4e00
	s_addc_u32 s39, s3, 0
	s_add_u32 s40, s2, 0x4f00
	s_addc_u32 s41, s3, 0
	s_add_u32 s42, s2, 0x5000
	s_addc_u32 s43, s3, 0
	s_add_u32 s44, s2, 0x5100
	s_addc_u32 s45, s3, 0
	s_add_u32 s46, s2, 0x5200
	s_addc_u32 s47, s3, 0
	s_waitcnt lgkmcnt(0)
	s_mul_i32 s0, s0, s78
	s_add_u32 s48, s2, 0x5300
	s_mul_i32 s0, s0, s1
	s_addc_u32 s49, s3, 0
	s_mov_b32 s1, 1
	v_mov_b32_e32 v17, 0
	s_branch .LBB0_300

; __device__ __forceinline__ void xcd_barrier(const XcdBarrier& b) {
;     asm volatile("s_waitcnt vmcnt(0)" ::: "memory");
;     __syncthreads();
;     if (threadIdx.x == 0) {
;         unsigned* bar = b.bar;
;         __builtin_amdgcn_s_waitcnt(0);
;         unsigned nloc = b.st[0], nx = b.st[1];
;         if (nloc == 0u) { xcd_barrier_complete(bar, b.x, nloc, nx); b.st[0] = nloc; b.st[1] = nx; }
.LBB0_379:
	s_or_b64 exec, exec, s[20:21]
	s_waitcnt vmcnt(0)
	s_barrier
	s_mov_b64 s[4:5], exec
	v_readlane_b32 s0, v252, 5
	v_readlane_b32 s1, v252, 6
	s_and_b64 s[0:1], s[4:5], s[0:1]
	s_mov_b64 exec, s[0:1]
	s_cbranch_execz .LBB0_431
	s_add_i32 s0, 0, 0x26c00
	v_mov_b32_e32 v1, s0
	s_waitcnt vmcnt(0) expcnt(0) lgkmcnt(0)
	buffer_wbl2 sc1
	ds_read_b32 v3, v1
	s_add_i32 s0, 0, 0x26c04
	v_mov_b32_e32 v1, s0
	ds_read_b32 v1, v1
	s_waitcnt lgkmcnt(1)
	v_cmp_ne_u32_e32 vcc, 0, v3
	s_cbranch_vccnz .LBB0_395
	v_readlane_b32 s2, v252, 7
	v_readlane_b32 s3, v252, 8
	s_load_dwordx2 s[0:1], s[2:3], 0x4
	v_readlane_b32 s2, v252, 0
	v_readlane_b32 s3, v252, 1
	s_add_u32 s6, s2, 0x4200
	s_addc_u32 s7, s3, 0
	s_add_u32 s8, s2, 0x4400
	s_addc_u32 s9, s3, 0
	s_add_u32 s10, s2, 0x4500
	s_addc_u32 s11, s3, 0
	s_add_u32 s12, s2, 0x4600
	s_addc_u32 s13, s3, 0
	s_add_u32 s14, s2, 0x4700
	s_addc_u32 s15, s3, 0
	s_add_u32 s16, s2, 0x4800
	s_addc_u32 s17, s3, 0
	s_add_u32 s18, s2, 0x4900
	s_addc_u32 s19, s3, 0
	s_add_u32 s20, s2, 0x4a00
	s_addc_u32 s21, s3, 0
	s_add_u32 s24, s2, 0x4b00
	s_addc_u32 s25, s3, 0
	s_add_u32 s34, s2, 0x4c00
	s_addc_u32 s35, s3, 0
	s_add_u32 s36, s2, 0x4d00
	s_addc_u32 s37, s3, 0
	s_add_u32 s38, s2, 0x4e00
	s_addc_u32 s39, s3, 0
	s_add_u32 s40, s2, 0x4f00
	s_addc_u32 s41, s3, 0
	s_add_u32 s42, s2, 0x5000
	s_addc_u32 s43, s3, 0
	s_add_u32 s44, s2, 0x5100
	s_addc_u32 s45, s3, 0
	s_add_u32 s46, s2, 0x5200
	s_addc_u32 s47, s3, 0
	s_waitcnt lgkmcnt(0)
	s_mul_i32 s0, s0, s78
	s_add_u32 s48, s2, 0x5300
	s_mul_i32 s0, s0, s1
	s_addc_u32 s49, s3, 0
	s_mov_b32 s1, 1
	v_mov_b32_e32 v17, 0
	s_branch .LBB0_383

; __device__ __forceinline__ void xcd_barrier(const XcdBarrier& b) {
;     asm volatile("s_waitcnt vmcnt(0)" ::: "memory");
;     __syncthreads();
;     if (threadIdx.x == 0) {
;         unsigned* bar = b.bar;
;         __builtin_amdgcn_s_waitcnt(0);
;         unsigned nloc = b.st[0], nx = b.st[1];
;         if (nloc == 0u) { xcd_barrier_complete(bar, b.x, nloc, nx); b.st[0] = nloc; b.st[1] = nx; }
.LBB0_589:
	s_waitcnt lgkmcnt(0)
	s_barrier
	s_waitcnt vmcnt(0)
	s_barrier
	s_mov_b64 s[4:5], exec
	v_readlane_b32 s0, v252, 5
	v_readlane_b32 s1, v252, 6
	s_and_b64 s[0:1], s[4:5], s[0:1]
	s_mov_b64 exec, s[0:1]
	s_cbranch_execz .LBB0_641
	s_add_i32 s0, 0, 0x26c00
	v_mov_b32_e32 v1, s0
	s_waitcnt vmcnt(0) expcnt(0) lgkmcnt(0)
	buffer_wbl2 sc1
	ds_read_b32 v3, v1
	s_add_i32 s0, 0, 0x26c04
	v_mov_b32_e32 v1, s0
	ds_read_b32 v1, v1
	s_waitcnt lgkmcnt(1)
	v_cmp_ne_u32_e32 vcc, 0, v3
	s_cbranch_vccnz .LBB0_605
	v_readlane_b32 s2, v252, 7
	v_readlane_b32 s3, v252, 8
	s_load_dwordx2 s[0:1], s[2:3], 0x4
	v_readlane_b32 s2, v252, 0
	v_readlane_b32 s3, v252, 1
	s_add_u32 s6, s2, 0x4200
	s_addc_u32 s7, s3, 0
	s_add_u32 s8, s2, 0x4400
	s_addc_u32 s9, s3, 0
	s_add_u32 s10, s2, 0x4500
	s_addc_u32 s11, s3, 0
	s_add_u32 s12, s2, 0x4600
	s_addc_u32 s13, s3, 0
	s_add_u32 s14, s2, 0x4700
	s_addc_u32 s15, s3, 0
	s_add_u32 s16, s2, 0x4800
	s_addc_u32 s17, s3, 0
	s_add_u32 s18, s2, 0x4900
	s_addc_u32 s19, s3, 0
	s_add_u32 s20, s2, 0x4a00
	s_addc_u32 s21, s3, 0
	s_add_u32 s24, s2, 0x4b00
	s_addc_u32 s25, s3, 0
	s_add_u32 s34, s2, 0x4c00
	s_addc_u32 s35, s3, 0
	s_add_u32 s36, s2, 0x4d00
	s_addc_u32 s37, s3, 0
	s_add_u32 s38, s2, 0x4e00
	s_addc_u32 s39, s3, 0
	s_add_u32 s40, s2, 0x4f00
	s_addc_u32 s41, s3, 0
	s_add_u32 s42, s2, 0x5000
	s_addc_u32 s43, s3, 0
	s_add_u32 s44, s2, 0x5100
	s_addc_u32 s45, s3, 0
	s_add_u32 s46, s2, 0x5200
	s_addc_u32 s47, s3, 0
	s_waitcnt lgkmcnt(0)
	s_mul_i32 s0, s0, s78
	s_add_u32 s48, s2, 0x5300
	s_mul_i32 s0, s0, s1
	s_addc_u32 s49, s3, 0
	s_mov_b32 s1, 1
	v_mov_b32_e32 v17, 0
	s_branch .LBB0_593

; __device__ __forceinline__ void xcd_barrier(const XcdBarrier& b) {
;     asm volatile("s_waitcnt vmcnt(0)" ::: "memory");
;     __syncthreads();
;     if (threadIdx.x == 0) {
;         unsigned* bar = b.bar;
;         __builtin_amdgcn_s_waitcnt(0);
;         unsigned nloc = b.st[0], nx = b.st[1];
;         if (nloc == 0u) { xcd_barrier_complete(bar, b.x, nloc, nx); b.st[0] = nloc; b.st[1] = nx; }
.LBB0_675:
	s_waitcnt vmcnt(0)
	s_waitcnt lgkmcnt(0)
	s_barrier
	s_mov_b64 s[4:5], exec
	v_readlane_b32 s0, v252, 5
	v_readlane_b32 s1, v252, 6
	s_and_b64 s[0:1], s[4:5], s[0:1]
	s_mov_b64 exec, s[0:1]
	s_cbranch_execz .LBB0_727
	s_add_i32 s0, 0, 0x26c00
	v_mov_b32_e32 v1, s0
	s_waitcnt vmcnt(0) expcnt(0) lgkmcnt(0)
	buffer_wbl2 sc1
	ds_read_b32 v3, v1
	s_add_i32 s0, 0, 0x26c04
	v_mov_b32_e32 v1, s0
	ds_read_b32 v1, v1
	s_waitcnt lgkmcnt(1)
	v_cmp_ne_u32_e32 vcc, 0, v3
	s_cbranch_vccnz .LBB0_691
	v_readlane_b32 s2, v252, 7
	v_readlane_b32 s3, v252, 8
	s_load_dwordx2 s[0:1], s[2:3], 0x4
	v_readlane_b32 s2, v252, 0
	v_readlane_b32 s3, v252, 1
	s_add_u32 s6, s2, 0x4200
	s_addc_u32 s7, s3, 0
	s_add_u32 s8, s2, 0x4400
	s_addc_u32 s9, s3, 0
	s_add_u32 s10, s2, 0x4500
	s_addc_u32 s11, s3, 0
	s_add_u32 s12, s2, 0x4600
	s_addc_u32 s13, s3, 0
	s_add_u32 s14, s2, 0x4700
	s_addc_u32 s15, s3, 0
	s_add_u32 s16, s2, 0x4800
	s_addc_u32 s17, s3, 0
	s_add_u32 s18, s2, 0x4900
	s_addc_u32 s19, s3, 0
	s_add_u32 s20, s2, 0x4a00
	s_addc_u32 s21, s3, 0
	s_add_u32 s24, s2, 0x4b00
	s_addc_u32 s25, s3, 0
	s_add_u32 s34, s2, 0x4c00
	s_addc_u32 s35, s3, 0
	s_add_u32 s36, s2, 0x4d00
	s_addc_u32 s37, s3, 0
	s_add_u32 s38, s2, 0x4e00
	s_addc_u32 s39, s3, 0
	s_add_u32 s40, s2, 0x4f00
	s_addc_u32 s41, s3, 0
	s_add_u32 s42, s2, 0x5000
	s_addc_u32 s43, s3, 0
	s_add_u32 s44, s2, 0x5100
	s_addc_u32 s45, s3, 0
	s_add_u32 s46, s2, 0x5200
	s_addc_u32 s47, s3, 0
	s_waitcnt lgkmcnt(0)
	s_mul_i32 s0, s0, s78
	s_add_u32 s48, s2, 0x5300
	s_mul_i32 s0, s0, s1
	s_addc_u32 s49, s3, 0
	s_mov_b32 s1, 1
	v_mov_b32_e32 v17, 0
	s_branch .LBB0_679

; __device__ __forceinline__ void xcd_barrier(const XcdBarrier& b) {
;     asm volatile("s_waitcnt vmcnt(0)" ::: "memory");
;     __syncthreads();
;     if (threadIdx.x == 0) {
;         unsigned* bar = b.bar;
;         __builtin_amdgcn_s_waitcnt(0);
;         unsigned nloc = b.st[0], nx = b.st[1];
;         if (nloc == 0u) { xcd_barrier_complete(bar, b.x, nloc, nx); b.st[0] = nloc; b.st[1] = nx; }
.LBB0_811:
	s_waitcnt vmcnt(0)
	s_barrier
	s_mov_b64 s[4:5], exec
	v_readlane_b32 s0, v252, 5
	v_readlane_b32 s1, v252, 6
	s_and_b64 s[0:1], s[4:5], s[0:1]
	s_mov_b64 exec, s[0:1]
	s_cbranch_execz .LBB0_863
	s_add_i32 s0, 0, 0x26c00
	v_mov_b32_e32 v1, s0
	s_waitcnt vmcnt(0) expcnt(0) lgkmcnt(0)
	buffer_wbl2 sc1
	ds_read_b32 v3, v1
	s_add_i32 s0, 0, 0x26c04
	v_mov_b32_e32 v1, s0
	ds_read_b32 v1, v1
	s_waitcnt lgkmcnt(1)
	v_cmp_ne_u32_e32 vcc, 0, v3
	s_cbranch_vccnz .LBB0_827
	v_readlane_b32 s2, v252, 7
	v_readlane_b32 s3, v252, 8
	s_load_dwordx2 s[0:1], s[2:3], 0x4
	v_readlane_b32 s2, v252, 0
	v_readlane_b32 s3, v252, 1
	s_add_u32 s6, s2, 0x4200
	s_addc_u32 s7, s3, 0
	s_add_u32 s8, s2, 0x4400
	s_addc_u32 s9, s3, 0
	s_add_u32 s10, s2, 0x4500
	s_addc_u32 s11, s3, 0
	s_add_u32 s12, s2, 0x4600
	s_addc_u32 s13, s3, 0
	s_add_u32 s14, s2, 0x4700
	s_addc_u32 s15, s3, 0
	s_add_u32 s16, s2, 0x4800
	s_addc_u32 s17, s3, 0
	s_add_u32 s18, s2, 0x4900
	s_addc_u32 s19, s3, 0
	s_add_u32 s20, s2, 0x4a00
	s_addc_u32 s21, s3, 0
	s_add_u32 s24, s2, 0x4b00
	s_addc_u32 s25, s3, 0
	s_add_u32 s34, s2, 0x4c00
	s_addc_u32 s35, s3, 0
	s_add_u32 s36, s2, 0x4d00
	s_addc_u32 s37, s3, 0
	s_add_u32 s38, s2, 0x4e00
	s_addc_u32 s39, s3, 0
	s_add_u32 s40, s2, 0x4f00
	s_addc_u32 s41, s3, 0
	s_add_u32 s42, s2, 0x5000
	s_addc_u32 s43, s3, 0
	s_add_u32 s44, s2, 0x5100
	s_addc_u32 s45, s3, 0
	s_add_u32 s46, s2, 0x5200
	s_addc_u32 s47, s3, 0
	s_waitcnt lgkmcnt(0)
	s_mul_i32 s0, s0, s78
	s_add_u32 s48, s2, 0x5300
	s_mul_i32 s0, s0, s1
	s_addc_u32 s49, s3, 0
	s_mov_b32 s1, 1
	v_mov_b32_e32 v17, 0
	s_branch .LBB0_815

; __device__ __forceinline__ void xcd_barrier(const XcdBarrier& b) {
;     asm volatile("s_waitcnt vmcnt(0)" ::: "memory");
;     __syncthreads();
;     if (threadIdx.x == 0) {
;         unsigned* bar = b.bar;
;         __builtin_amdgcn_s_waitcnt(0);
;         unsigned nloc = b.st[0], nx = b.st[1];
;         if (nloc == 0u) { xcd_barrier_complete(bar, b.x, nloc, nx); b.st[0] = nloc; b.st[1] = nx; }
.LBB0_1089:
	s_waitcnt vmcnt(0)
	s_waitcnt vmcnt(0) lgkmcnt(0)
	s_barrier
	s_mov_b64 s[4:5], exec
	v_readlane_b32 s0, v252, 5
	v_readlane_b32 s1, v252, 6
	s_and_b64 s[0:1], s[4:5], s[0:1]
	s_mov_b64 exec, s[0:1]
	s_cbranch_execz .LBB0_1141
	s_add_i32 s0, 0, 0x26c00
	v_mov_b32_e32 v1, s0
	s_waitcnt vmcnt(0) expcnt(0) lgkmcnt(0)
	buffer_wbl2 sc1
	ds_read_b32 v3, v1
	s_add_i32 s0, 0, 0x26c04
	v_mov_b32_e32 v1, s0
	ds_read_b32 v1, v1
	s_waitcnt lgkmcnt(1)
	v_cmp_ne_u32_e32 vcc, 0, v3
	s_cbranch_vccnz .LBB0_1105
	v_readlane_b32 s2, v252, 7
	v_readlane_b32 s3, v252, 8
	s_load_dwordx2 s[0:1], s[2:3], 0x4
	v_readlane_b32 s2, v252, 0
	v_readlane_b32 s3, v252, 1
	s_add_u32 s6, s2, 0x4200
	s_addc_u32 s7, s3, 0
	s_add_u32 s8, s2, 0x4400
	s_addc_u32 s9, s3, 0
	s_add_u32 s10, s2, 0x4500
	s_addc_u32 s11, s3, 0
	s_add_u32 s12, s2, 0x4600
	s_addc_u32 s13, s3, 0
	s_add_u32 s14, s2, 0x4700
	s_addc_u32 s15, s3, 0
	s_add_u32 s16, s2, 0x4800
	s_addc_u32 s17, s3, 0
	s_add_u32 s18, s2, 0x4900
	s_addc_u32 s19, s3, 0
	s_add_u32 s20, s2, 0x4a00
	s_addc_u32 s21, s3, 0
	s_add_u32 s24, s2, 0x4b00
	s_addc_u32 s25, s3, 0
	s_add_u32 s34, s2, 0x4c00
	s_addc_u32 s35, s3, 0
	s_add_u32 s36, s2, 0x4d00
	s_addc_u32 s37, s3, 0
	s_add_u32 s38, s2, 0x4e00
	s_addc_u32 s39, s3, 0
	s_add_u32 s40, s2, 0x4f00
	s_addc_u32 s41, s3, 0
	s_add_u32 s42, s2, 0x5000
	s_addc_u32 s43, s3, 0
	s_add_u32 s44, s2, 0x5100
	s_addc_u32 s45, s3, 0
	s_add_u32 s46, s2, 0x5200
	s_addc_u32 s47, s3, 0
	s_waitcnt lgkmcnt(0)
	s_mul_i32 s0, s0, s78
	s_add_u32 s48, s2, 0x5300
	s_mul_i32 s0, s0, s1
	s_addc_u32 s49, s3, 0
	s_mov_b32 s1, 1
	v_mov_b32_e32 v17, 0
	s_branch .LBB0_1093

; __device__ __forceinline__ void xcd_barrier(const XcdBarrier& b) {
;     asm volatile("s_waitcnt vmcnt(0)" ::: "memory");
;     __syncthreads();
;     if (threadIdx.x == 0) {
;         unsigned* bar = b.bar;
;         __builtin_amdgcn_s_waitcnt(0);
;         unsigned nloc = b.st[0], nx = b.st[1];
;         if (nloc == 0u) { xcd_barrier_complete(bar, b.x, nloc, nx); b.st[0] = nloc; b.st[1] = nx; }
.LBB0_1983:
	s_waitcnt vmcnt(0)
	s_waitcnt vmcnt(0) lgkmcnt(0)
	s_barrier
	s_mov_b64 s[4:5], exec
	v_readlane_b32 s0, v252, 5
	v_readlane_b32 s1, v252, 6
	s_and_b64 s[0:1], s[4:5], s[0:1]
	s_mov_b64 exec, s[0:1]
	s_cbranch_execz .LBB0_2035
	s_add_i32 s0, 0, 0x26c00
	v_mov_b32_e32 v1, s0
	s_waitcnt vmcnt(0) expcnt(0) lgkmcnt(0)
	buffer_wbl2 sc1
	ds_read_b32 v3, v1
	s_add_i32 s0, 0, 0x26c04
	v_mov_b32_e32 v1, s0
	ds_read_b32 v1, v1
	s_waitcnt lgkmcnt(1)
	v_cmp_ne_u32_e32 vcc, 0, v3
	s_cbranch_vccnz .LBB0_1999
	v_readlane_b32 s2, v252, 7
	v_readlane_b32 s3, v252, 8
	s_load_dwordx2 s[0:1], s[2:3], 0x4
	v_readlane_b32 s2, v252, 0
	v_readlane_b32 s3, v252, 1
	s_add_u32 s6, s2, 0x4200
	s_addc_u32 s7, s3, 0
	s_add_u32 s8, s2, 0x4400
	s_addc_u32 s9, s3, 0
	s_add_u32 s10, s2, 0x4500
	s_addc_u32 s11, s3, 0
	s_add_u32 s12, s2, 0x4600
	s_addc_u32 s13, s3, 0
	s_add_u32 s14, s2, 0x4700
	s_addc_u32 s15, s3, 0
	s_add_u32 s16, s2, 0x4800
	s_addc_u32 s17, s3, 0
	s_add_u32 s18, s2, 0x4900
	s_addc_u32 s19, s3, 0
	s_add_u32 s20, s2, 0x4a00
	s_addc_u32 s21, s3, 0
	s_add_u32 s22, s2, 0x4b00
	s_addc_u32 s23, s3, 0
	s_add_u32 s24, s2, 0x4c00
	s_addc_u32 s25, s3, 0
	s_add_u32 s30, s2, 0x4d00
	s_addc_u32 s31, s3, 0
	s_add_u32 s34, s2, 0x4e00
	s_addc_u32 s35, s3, 0
	s_add_u32 s36, s2, 0x4f00
	s_addc_u32 s37, s3, 0
	s_add_u32 s38, s2, 0x5000
	s_addc_u32 s39, s3, 0
	s_add_u32 s40, s2, 0x5100
	s_addc_u32 s41, s3, 0
	s_add_u32 s42, s2, 0x5200
	s_addc_u32 s43, s3, 0
	s_waitcnt lgkmcnt(0)
	s_mul_i32 s0, s0, s78
	s_add_u32 s44, s2, 0x5300
	s_mul_i32 s0, s0, s1
	s_addc_u32 s45, s3, 0
	s_mov_b32 s1, 1
	v_mov_b32_e32 v17, 0
	s_branch .LBB0_1987
